# grid barrier: last XCD leader releases all XCD generation words directly (one hop fewer), leader acquire beside its write-back; E1 next-unit token offsets deferred past first K-trip; E2 gate load hois
# speedup vs baseline: 1.0253x; 1.0133x over previous
.LBB0_102:
	s_andn2_saveexec_b64 s[6:7], s[6:7]
	s_cbranch_execz .LBB0_122
	s_mov_b64 s[6:7], exec
	buffer_wbl2 sc1
	buffer_inv sc1
	s_waitcnt lgkmcnt(0)
	s_waitcnt vmcnt(0)
	v_mbcnt_lo_u32_b32 v1, s6, 0
	v_mbcnt_hi_u32_b32 v1, s7, v1
	v_cmp_eq_u32_e32 vcc, 0, v1
	s_and_saveexec_b64 s[8:9], vcc
	s_cbranch_execz .LBB0_105
	s_bcnt1_i32_b64 s3, s[6:7]
	v_mov_b32_e32 v2, 0x3000
	v_mov_b32_e32 v3, s3
	global_atomic_add v2, v2, v3, s[4:5] offset:1024 sc0

.LBB0_117:
	s_or_b64 exec, exec, s[6:7]
	s_and_saveexec_b64 s[6:7], s[10:11]
	s_cbranch_execz .LBB0_119
	v_mov_b32_e32 v2, 1
	global_atomic_add v[0:1], v2, off
	s_add_u32 s2, s4, 0x2400
	s_addc_u32 s3, s5, 0
	v_mov_b32_e32 v4, 0
	v_mov_b32_e32 v5, 1
	global_atomic_add v4, v5, s[2:3]
	global_atomic_add v4, v5, s[2:3] offset:256
	global_atomic_add v4, v5, s[2:3] offset:512
	global_atomic_add v4, v5, s[2:3] offset:768
	global_atomic_add v4, v5, s[2:3] offset:1024
	global_atomic_add v4, v5, s[2:3] offset:1280
	global_atomic_add v4, v5, s[2:3] offset:1536
	global_atomic_add v4, v5, s[2:3] offset:1792
	global_atomic_add v4, v5, s[2:3] offset:2048
	global_atomic_add v4, v5, s[2:3] offset:2304
	global_atomic_add v4, v5, s[2:3] offset:2560
	global_atomic_add v4, v5, s[2:3] offset:2816
	global_atomic_add v4, v5, s[2:3] offset:3072
	global_atomic_add v4, v5, s[2:3] offset:3328
	global_atomic_add v4, v5, s[2:3] offset:3584
	global_atomic_add v4, v5, s[2:3] offset:3840
.LBB0_119:
	s_or_b64 exec, exec, s[6:7]
	s_mov_b64 s[6:7], exec
	v_mbcnt_lo_u32_b32 v0, s6, 0
	v_mbcnt_hi_u32_b32 v0, s7, v0
	s_mov_b32 s11, 0
	v_cmp_eq_u32_e32 vcc, 0, v0
	s_waitcnt vmcnt(0)
	s_and_saveexec_b64 s[8:9], vcc
	s_cbranch_execz .LBB0_121

.LBB0_206:
	s_andn2_saveexec_b64 s[6:7], s[6:7]
	s_cbranch_execz .LBB0_226
	s_mov_b64 s[6:7], exec
	buffer_wbl2 sc1
	buffer_inv sc1
	s_waitcnt lgkmcnt(0)
	s_waitcnt vmcnt(0)
	v_mbcnt_lo_u32_b32 v1, s6, 0
	v_mbcnt_hi_u32_b32 v1, s7, v1
	v_cmp_eq_u32_e32 vcc, 0, v1
	s_and_saveexec_b64 s[8:9], vcc
	s_cbranch_execz .LBB0_209
	s_bcnt1_i32_b64 s3, s[6:7]
	v_mov_b32_e32 v3, s3
	v_mov_b32_e32 v4, 0x3000
	global_atomic_add v3, v4, v3, s[4:5] offset:1024 sc0

.LBB0_221:
	s_or_b64 exec, exec, s[8:9]
	s_and_saveexec_b64 s[6:7], s[12:13]
	s_cbranch_execz .LBB0_223
	v_mov_b32_e32 v1, 1
	global_atomic_add v[2:3], v1, off
	s_add_u32 s2, s4, 0x2400
	s_addc_u32 s3, s5, 0
	v_mov_b32_e32 v4, 0
	v_mov_b32_e32 v5, 1
	global_atomic_add v4, v5, s[2:3]
	global_atomic_add v4, v5, s[2:3] offset:256
	global_atomic_add v4, v5, s[2:3] offset:512
	global_atomic_add v4, v5, s[2:3] offset:768
	global_atomic_add v4, v5, s[2:3] offset:1024
	global_atomic_add v4, v5, s[2:3] offset:1280
	global_atomic_add v4, v5, s[2:3] offset:1536
	global_atomic_add v4, v5, s[2:3] offset:1792
	global_atomic_add v4, v5, s[2:3] offset:2048
	global_atomic_add v4, v5, s[2:3] offset:2304
	global_atomic_add v4, v5, s[2:3] offset:2560
	global_atomic_add v4, v5, s[2:3] offset:2816
	global_atomic_add v4, v5, s[2:3] offset:3072
	global_atomic_add v4, v5, s[2:3] offset:3328
	global_atomic_add v4, v5, s[2:3] offset:3584
	global_atomic_add v4, v5, s[2:3] offset:3840
.LBB0_223:
	s_or_b64 exec, exec, s[6:7]
	s_mov_b64 s[6:7], exec
	v_mbcnt_lo_u32_b32 v1, s6, 0
	v_mbcnt_hi_u32_b32 v1, s7, v1
	v_cmp_eq_u32_e32 vcc, 0, v1
	s_waitcnt vmcnt(0)
	s_and_saveexec_b64 s[8:9], vcc
	s_cbranch_execz .LBB0_225

.LBB0_430:
	s_waitcnt lgkmcnt(0)
	v_mfma_scale_f32_32x32x64_f8f6f4 v[144:159], v[184:191], v[192:199], v[96:111], v207, v218 op_sel_hi:[0,0,0]
	ds_read_b128 v[2:5], v221
	ds_read_b128 v[184:187], v221 offset:2048
	ds_read_b128 v[6:9], v222
	ds_read_b128 v[168:171], v221 offset:4096
	ds_read_b128 v[188:191], v222 offset:2048
	ds_read_b128 v[172:175], v222 offset:4096
	v_cvt_pknorm_u16_f32 v1, v112, v113
	v_cvt_pknorm_u16_f32 v10, v114, v115
	v_perm_b32 v160, v10, v1, s55
	v_cvt_pknorm_u16_f32 v1, v116, v117
	v_cvt_pknorm_u16_f32 v10, v118, v119
	v_perm_b32 v161, v10, v1, s55
	v_cvt_pknorm_u16_f32 v1, v120, v121
	v_cvt_pknorm_u16_f32 v10, v122, v123
	v_perm_b32 v162, v10, v1, s55
	v_cvt_pknorm_u16_f32 v1, v124, v125
	v_cvt_pknorm_u16_f32 v10, v126, v127
	v_perm_b32 v163, v10, v1, s55
	s_waitcnt lgkmcnt(6)
	v_mfma_scale_f32_32x32x64_f8f6f4 v[112:127], v[176:183], v[192:199], v[96:111], v207, v218 op_sel_hi:[0,0,0]
	s_add_u32 s52, s4, s84
	s_addc_u32 s54, s5, s85
	s_add_u32 s14, s52, 0xa000
	s_addc_u32 s15, s54, 0
	v_cvt_pknorm_u16_f32 v1, v128, v129
	v_cvt_pknorm_u16_f32 v10, v130, v131
	s_add_u32 s56, s6, s84
	v_perm_b32 v164, v10, v1, s55
	v_cvt_pknorm_u16_f32 v1, v132, v133
	v_cvt_pknorm_u16_f32 v10, v134, v135
	s_addc_u32 s61, s7, s85
	v_perm_b32 v165, v10, v1, s55
	v_cvt_pknorm_u16_f32 v1, v136, v137
	v_cvt_pknorm_u16_f32 v10, v138, v139
	s_add_u32 s20, s56, 0xa000
	v_perm_b32 v166, v10, v1, s55
	v_cvt_pknorm_u16_f32 v1, v140, v141
	v_cvt_pknorm_u16_f32 v10, v142, v143
	s_addc_u32 s21, s61, 0
	v_perm_b32 v167, v10, v1, s55
	s_mov_b32 m0, s45
	v_lshl_add_u64 v[10:11], s[14:15], 0, v[200:201]
	global_load_lds_dwordx4 v[10:11], off
	v_lshl_add_u64 v[10:11], s[20:21], 0, v[202:203]
	s_add_i32 m0, s23, 0xc800
	s_nop 0
	global_load_lds_dwordx4 v[10:11], off
	s_waitcnt lgkmcnt(0)
	v_mfma_scale_f32_32x32x64_f8f6f4 v[64:79], v[2:9], v[160:167], v[64:79], v207, v207 op_sel_hi:[0,0,0]
	ds_read_b128 v[136:139], v221 offset:6144
	ds_read_b128 v[140:143], v222 offset:6144
	v_mfma_scale_f32_32x32x64_f8f6f4 v[48:63], v[184:191], v[160:167], v[48:63], v207, v207 op_sel_hi:[0,0,0]
	ds_read_b128 v[176:179], v221 offset:8192
	ds_read_b128 v[180:183], v222 offset:8192
	ds_read_b128 v[128:131], v219 offset:16384
	ds_read_b128 v[2:5], v219 offset:20480
	ds_read_b128 v[132:135], v220 offset:16384
	ds_read_b128 v[6:9], v220 offset:20480
	v_mov_b32_e32 v1, v144
	v_max3_f32 v1, v1, v144, v145
	v_max3_f32 v1, v1, v146, v147
	v_max3_f32 v1, v1, v148, v149
	v_max3_f32 v1, v1, v150, v151
	v_max3_f32 v1, v1, v152, v153
	v_max3_f32 v1, v1, v154, v155
	v_max3_f32 v1, v1, v156, v157
	v_max3_f32 v1, v1, v158, v159
	v_mfma_scale_f32_32x32x64_f8f6f4 v[32:47], v[168:175], v[160:167], v[32:47], v207, v207 op_sel_hi:[0,0,0]
	v_max3_f32 v1, v1, v112, v113
	v_max3_f32 v1, v1, v114, v115
	v_max3_f32 v1, v1, v116, v117
	v_max3_f32 v1, v1, v118, v119
	v_max3_f32 v1, v1, v120, v121
	v_max3_f32 v1, v1, v122, v123
	v_max3_f32 v1, v1, v124, v125
	v_max3_f32 v1, v1, v126, v127
	v_cmp_ge_f32_e32 vcc, s53, v1
	s_cmp_eq_u64 vcc, exec
	s_waitcnt lgkmcnt(0)
	v_mfma_scale_f32_32x32x64_f8f6f4 v[16:31], v[136:143], v[160:167], v[16:31], v207, v207 op_sel_hi:[0,0,0]
	v_mfma_scale_f32_32x32x64_f8f6f4 v[80:95], v[176:183], v[160:167], v[80:95], v207, v207 op_sel_hi:[0,0,0]
	s_cbranch_scc0 .LBB0_438
.LBB0_431:
	s_waitcnt vmcnt(4)
	s_waitcnt lgkmcnt(0)
	s_barrier
	v_mfma_scale_f32_32x32x64_f8f6f4 v[160:175], v[128:135], v[192:199], v[96:111], v207, v218 op_sel_hi:[0,0,0]
	ds_read_b128 v[224:227], v221 offset:10240
	ds_read_b128 v[232:235], v221 offset:12288
	ds_read_b128 v[228:231], v222 offset:10240
	ds_read_b128 v[136:139], v221 offset:14336
	ds_read_b128 v[236:239], v222 offset:12288
	ds_read_b128 v[140:143], v222 offset:14336
	v_cvt_pknorm_u16_f32 v1, v144, v145
	v_cvt_pknorm_u16_f32 v10, v146, v147
	v_perm_b32 v128, v10, v1, s55
	v_cvt_pknorm_u16_f32 v1, v148, v149
	v_cvt_pknorm_u16_f32 v10, v150, v151
	v_perm_b32 v129, v10, v1, s55
	v_cvt_pknorm_u16_f32 v1, v152, v153
	v_cvt_pknorm_u16_f32 v10, v154, v155
	v_perm_b32 v130, v10, v1, s55
	v_cvt_pknorm_u16_f32 v1, v156, v157
	v_cvt_pknorm_u16_f32 v10, v158, v159
	v_perm_b32 v131, v10, v1, s55
	v_mfma_scale_f32_32x32x64_f8f6f4 v[176:191], v[2:9], v[192:199], v[96:111], v207, v218 op_sel_hi:[0,0,0]
	v_cvt_pknorm_u16_f32 v1, v112, v113
	v_cvt_pknorm_u16_f32 v2, v114, v115
	s_add_u32 s14, s52, 0xc000
	v_perm_b32 v132, v2, v1, s55
	v_cvt_pknorm_u16_f32 v1, v116, v117
	v_cvt_pknorm_u16_f32 v2, v118, v119
	s_addc_u32 s15, s54, 0
	v_perm_b32 v133, v2, v1, s55
	v_cvt_pknorm_u16_f32 v1, v120, v121
	v_cvt_pknorm_u16_f32 v2, v122, v123
	s_add_u32 s20, s56, 0xc000
	v_perm_b32 v134, v2, v1, s55
	v_cvt_pknorm_u16_f32 v1, v124, v125
	v_cvt_pknorm_u16_f32 v2, v126, v127
	s_addc_u32 s21, s61, 0
	v_perm_b32 v135, v2, v1, s55
	s_mov_b32 m0, s59
	v_lshl_add_u64 v[2:3], s[14:15], 0, v[200:201]
	global_load_lds_dwordx4 v[2:3], off
	v_lshl_add_u64 v[2:3], s[20:21], 0, v[202:203]
	s_mov_b32 m0, s23
	s_nop 0
	global_load_lds_dwordx4 v[2:3], off
	s_waitcnt lgkmcnt(0)
	v_mfma_scale_f32_32x32x64_f8f6f4 v[64:79], v[224:231], v[128:135], v[64:79], v207, v207 op_sel_hi:[0,0,0]
	ds_read_b128 v[120:123], v221 offset:16384
	ds_read_b128 v[124:127], v222 offset:16384
	v_mfma_scale_f32_32x32x64_f8f6f4 v[48:63], v[232:239], v[128:135], v[48:63], v207, v207 op_sel_hi:[0,0,0]
	ds_read_b128 v[144:147], v221 offset:18432
	ds_read_b128 v[148:151], v222 offset:18432
	ds_read_b128 v[112:115], v219 offset:24576
	ds_read_b128 v[2:5], v219 offset:28672
	ds_read_b128 v[116:119], v220 offset:24576
	ds_read_b128 v[6:9], v220 offset:28672
	v_mov_b32_e32 v1, v160
	v_max3_f32 v1, v1, v160, v161
	v_max3_f32 v1, v1, v162, v163
	v_max3_f32 v1, v1, v164, v165
	v_max3_f32 v1, v1, v166, v167
	v_max3_f32 v1, v1, v168, v169
	v_max3_f32 v1, v1, v170, v171
	v_max3_f32 v1, v1, v172, v173
	v_max3_f32 v1, v1, v174, v175
	v_mfma_scale_f32_32x32x64_f8f6f4 v[32:47], v[136:143], v[128:135], v[32:47], v207, v207 op_sel_hi:[0,0,0]
	v_max3_f32 v1, v1, v176, v177
	v_max3_f32 v1, v1, v178, v179
	v_max3_f32 v1, v1, v180, v181
	v_max3_f32 v1, v1, v182, v183
	v_max3_f32 v1, v1, v184, v185
	v_max3_f32 v1, v1, v186, v187
	v_max3_f32 v1, v1, v188, v189
	v_max3_f32 v1, v1, v190, v191
	v_cmp_ge_f32_e32 vcc, s53, v1
	s_cmp_eq_u64 vcc, exec
	s_waitcnt lgkmcnt(0)
	v_mfma_scale_f32_32x32x64_f8f6f4 v[16:31], v[120:127], v[128:135], v[16:31], v207, v207 op_sel_hi:[0,0,0]
	v_mfma_scale_f32_32x32x64_f8f6f4 v[80:95], v[144:151], v[128:135], v[80:95], v207, v207 op_sel_hi:[0,0,0]
	s_cbranch_scc0 .LBB0_441
.LBB0_432:
	s_waitcnt vmcnt(4)
	s_waitcnt lgkmcnt(0)
	s_barrier
	v_mfma_scale_f32_32x32x64_f8f6f4 v[128:143], v[112:119], v[192:199], v[96:111], v207, v218 op_sel_hi:[0,0,0]
	ds_read_b128 v[224:227], v221 offset:20480
	ds_read_b128 v[232:235], v221 offset:22528
	ds_read_b128 v[228:231], v222 offset:20480
	ds_read_b128 v[120:123], v221 offset:24576
	ds_read_b128 v[236:239], v222 offset:22528
	ds_read_b128 v[124:127], v222 offset:24576
	v_cvt_pknorm_u16_f32 v1, v160, v161
	v_cvt_pknorm_u16_f32 v10, v162, v163
	v_perm_b32 v112, v10, v1, s55
	v_cvt_pknorm_u16_f32 v1, v164, v165
	v_cvt_pknorm_u16_f32 v10, v166, v167
	v_perm_b32 v113, v10, v1, s55
	v_cvt_pknorm_u16_f32 v1, v168, v169
	v_cvt_pknorm_u16_f32 v10, v170, v171
	v_perm_b32 v114, v10, v1, s55
	v_cvt_pknorm_u16_f32 v1, v172, v173
	v_cvt_pknorm_u16_f32 v10, v174, v175
	v_perm_b32 v115, v10, v1, s55
	v_mfma_scale_f32_32x32x64_f8f6f4 v[144:159], v[2:9], v[192:199], v[96:111], v207, v218 op_sel_hi:[0,0,0]
	v_cvt_pknorm_u16_f32 v1, v176, v177
	v_cvt_pknorm_u16_f32 v2, v178, v179
	s_add_u32 s14, s52, 0xe000
	v_perm_b32 v116, v2, v1, s55
	v_cvt_pknorm_u16_f32 v1, v180, v181
	v_cvt_pknorm_u16_f32 v2, v182, v183
	s_addc_u32 s15, s54, 0
	v_perm_b32 v117, v2, v1, s55
	v_cvt_pknorm_u16_f32 v1, v184, v185
	v_cvt_pknorm_u16_f32 v2, v186, v187
	s_add_u32 s20, s56, 0xe000
	v_perm_b32 v118, v2, v1, s55
	v_cvt_pknorm_u16_f32 v1, v188, v189
	v_cvt_pknorm_u16_f32 v2, v190, v191
	s_addc_u32 s21, s61, 0
	v_perm_b32 v119, v2, v1, s55
	s_mov_b32 m0, s48
	v_lshl_add_u64 v[2:3], s[14:15], 0, v[200:201]
	global_load_lds_dwordx4 v[2:3], off
	v_lshl_add_u64 v[2:3], s[20:21], 0, v[202:203]
	s_mov_b32 m0, s2
	s_nop 0
	global_load_lds_dwordx4 v[2:3], off
	s_waitcnt lgkmcnt(0)
	v_mfma_scale_f32_32x32x64_f8f6f4 v[64:79], v[224:231], v[112:119], v[64:79], v207, v207 op_sel_hi:[0,0,0]
	ds_read_b128 v[168:171], v221 offset:26624
	ds_read_b128 v[172:175], v222 offset:26624
	v_mfma_scale_f32_32x32x64_f8f6f4 v[48:63], v[232:239], v[112:119], v[48:63], v207, v207 op_sel_hi:[0,0,0]
	ds_read_b128 v[176:179], v221 offset:28672
	ds_read_b128 v[180:183], v222 offset:28672
	ds_read_b128 v[160:163], v219 offset:32768
	ds_read_b128 v[2:5], v219 offset:36864
	ds_read_b128 v[164:167], v220 offset:32768
	ds_read_b128 v[6:9], v220 offset:36864
	v_mov_b32_e32 v1, v128
	v_max3_f32 v1, v1, v128, v129
	v_max3_f32 v1, v1, v130, v131
	v_max3_f32 v1, v1, v132, v133
	v_max3_f32 v1, v1, v134, v135
	v_max3_f32 v1, v1, v136, v137
	v_max3_f32 v1, v1, v138, v139
	v_max3_f32 v1, v1, v140, v141
	v_max3_f32 v1, v1, v142, v143
	v_mfma_scale_f32_32x32x64_f8f6f4 v[32:47], v[120:127], v[112:119], v[32:47], v207, v207 op_sel_hi:[0,0,0]
	v_max3_f32 v1, v1, v144, v145
	v_max3_f32 v1, v1, v146, v147
	v_max3_f32 v1, v1, v148, v149
	v_max3_f32 v1, v1, v150, v151
	v_max3_f32 v1, v1, v152, v153
	v_max3_f32 v1, v1, v154, v155
	v_max3_f32 v1, v1, v156, v157
	v_max3_f32 v1, v1, v158, v159
	v_cmp_ge_f32_e32 vcc, s53, v1
	s_cmp_eq_u64 vcc, exec
	s_waitcnt lgkmcnt(0)
	v_mfma_scale_f32_32x32x64_f8f6f4 v[16:31], v[168:175], v[112:119], v[16:31], v207, v207 op_sel_hi:[0,0,0]
	v_mfma_scale_f32_32x32x64_f8f6f4 v[80:95], v[176:183], v[112:119], v[80:95], v207, v207 op_sel_hi:[0,0,0]
	s_cbranch_scc0 .LBB0_444
.LBB0_433:
	s_waitcnt vmcnt(4)
	s_waitcnt lgkmcnt(0)
	s_barrier
	v_mfma_scale_f32_32x32x64_f8f6f4 v[112:127], v[160:167], v[192:199], v[96:111], v207, v218 op_sel_hi:[0,0,0]
	ds_read_b128 v[184:187], v221 offset:30720
	ds_read_b128 v[228:231], v222 offset:32768
	ds_read_b128 v[224:227], v221 offset:32768
	ds_read_b128 v[176:179], v221 offset:34816
	ds_read_b128 v[188:191], v222 offset:30720
	ds_read_b128 v[180:183], v222 offset:34816
	v_cvt_pknorm_u16_f32 v1, v128, v129
	v_cvt_pknorm_u16_f32 v10, v130, v131
	v_perm_b32 v128, v10, v1, s55
	v_cvt_pknorm_u16_f32 v1, v132, v133
	v_cvt_pknorm_u16_f32 v10, v134, v135
	v_perm_b32 v129, v10, v1, s55
	v_cvt_pknorm_u16_f32 v1, v136, v137
	v_cvt_pknorm_u16_f32 v10, v138, v139
	v_perm_b32 v130, v10, v1, s55
	v_cvt_pknorm_u16_f32 v1, v140, v141
	v_cvt_pknorm_u16_f32 v10, v142, v143
	v_perm_b32 v131, v10, v1, s55
	v_mfma_scale_f32_32x32x64_f8f6f4 v[160:175], v[2:9], v[192:199], v[96:111], v207, v218 op_sel_hi:[0,0,0]
	s_add_i32 s14, s33, -2
	s_min_u32 s14, s14, s17
	s_lshl_b32 s20, s14, 13
	v_cvt_pknorm_u16_f32 v1, v144, v145
	v_cvt_pknorm_u16_f32 v2, v146, v147
	s_add_u32 s14, s4, s20
	v_perm_b32 v132, v2, v1, s55
	v_cvt_pknorm_u16_f32 v1, v148, v149
	v_cvt_pknorm_u16_f32 v2, v150, v151
	s_addc_u32 s15, s5, 0
	v_perm_b32 v133, v2, v1, s55
	v_cvt_pknorm_u16_f32 v1, v152, v153
	v_cvt_pknorm_u16_f32 v2, v154, v155
	s_add_u32 s20, s6, s20
	v_perm_b32 v134, v2, v1, s55
	v_cvt_pknorm_u16_f32 v1, v156, v157
	v_cvt_pknorm_u16_f32 v2, v158, v159
	s_addc_u32 s21, s7, 0
	v_perm_b32 v135, v2, v1, s55
	s_mov_b32 m0, s49
	v_lshl_add_u64 v[2:3], s[14:15], 0, v[200:201]
	global_load_lds_dwordx4 v[2:3], off
	v_lshl_add_u64 v[2:3], s[20:21], 0, v[202:203]
	s_mov_b32 m0, s3
	s_nop 0
	global_load_lds_dwordx4 v[2:3], off
	s_waitcnt lgkmcnt(0)
	v_mfma_scale_f32_32x32x64_f8f6f4 v[64:79], v[184:191], v[128:135], v[64:79], v207, v207 op_sel_hi:[0,0,0]
	ds_read_b128 v[136:139], v221 offset:36864
	ds_read_b128 v[140:143], v222 offset:36864
	v_mfma_scale_f32_32x32x64_f8f6f4 v[48:63], v[224:231], v[128:135], v[48:63], v207, v207 op_sel_hi:[0,0,0]
	ds_read_b128 v[152:155], v221 offset:38912
	ds_read_b128 v[156:159], v222 offset:38912
	ds_read_b128 v[144:147], v219 offset:40960
	ds_read_b128 v[2:5], v219 offset:45056
	ds_read_b128 v[148:151], v220 offset:40960
	ds_read_b128 v[6:9], v220 offset:45056
	v_mov_b32_e32 v1, v112
	v_max3_f32 v1, v1, v112, v113
	v_max3_f32 v1, v1, v114, v115
	v_max3_f32 v1, v1, v116, v117
	v_max3_f32 v1, v1, v118, v119
	v_max3_f32 v1, v1, v120, v121
	v_max3_f32 v1, v1, v122, v123
	v_max3_f32 v1, v1, v124, v125
	v_max3_f32 v1, v1, v126, v127
	v_mfma_scale_f32_32x32x64_f8f6f4 v[32:47], v[176:183], v[128:135], v[32:47], v207, v207 op_sel_hi:[0,0,0]
	v_max3_f32 v1, v1, v160, v161
	v_max3_f32 v1, v1, v162, v163
	v_max3_f32 v1, v1, v164, v165
	v_max3_f32 v1, v1, v166, v167
	v_max3_f32 v1, v1, v168, v169
	v_max3_f32 v1, v1, v170, v171
	v_max3_f32 v1, v1, v172, v173
	v_max3_f32 v1, v1, v174, v175
	v_cmp_ge_f32_e32 vcc, s53, v1
	s_cmp_eq_u64 vcc, exec
	s_waitcnt lgkmcnt(0)
	v_mfma_scale_f32_32x32x64_f8f6f4 v[16:31], v[136:143], v[128:135], v[16:31], v207, v207 op_sel_hi:[0,0,0]
	v_mfma_scale_f32_32x32x64_f8f6f4 v[80:95], v[152:159], v[128:135], v[80:95], v207, v207 op_sel_hi:[0,0,0]
	s_cbranch_scc0 .LBB0_447
.LBB0_434:
	s_waitcnt vmcnt(4)
	s_waitcnt lgkmcnt(0)
	s_barrier
	v_mfma_scale_f32_32x32x64_f8f6f4 v[128:143], v[144:151], v[192:199], v[96:111], v207, v218 op_sel_hi:[0,0,0]
	ds_read_b128 v[184:187], v221 offset:40960
	ds_read_b128 v[224:227], v221 offset:43008
	ds_read_b128 v[188:191], v222 offset:40960
	ds_read_b128 v[176:179], v221 offset:45056
	ds_read_b128 v[228:231], v222 offset:43008
	ds_read_b128 v[180:183], v222 offset:45056
	v_cvt_pknorm_u16_f32 v1, v112, v113
	v_cvt_pknorm_u16_f32 v10, v114, v115
	v_perm_b32 v112, v10, v1, s55
	v_cvt_pknorm_u16_f32 v1, v116, v117
	v_cvt_pknorm_u16_f32 v10, v118, v119
	v_perm_b32 v113, v10, v1, s55
	v_cvt_pknorm_u16_f32 v1, v120, v121
	v_cvt_pknorm_u16_f32 v10, v122, v123
	v_perm_b32 v114, v10, v1, s55
	v_cvt_pknorm_u16_f32 v1, v124, v125
	v_cvt_pknorm_u16_f32 v10, v126, v127
	v_perm_b32 v115, v10, v1, s55
	v_mfma_scale_f32_32x32x64_f8f6f4 v[144:159], v[2:9], v[192:199], v[96:111], v207, v218 op_sel_hi:[0,0,0]
	s_add_i32 s14, s33, -1
	s_min_u32 s14, s14, s17
	s_lshl_b32 s20, s14, 13
	v_cvt_pknorm_u16_f32 v1, v160, v161
	v_cvt_pknorm_u16_f32 v2, v162, v163
	s_add_u32 s14, s4, s20
	v_perm_b32 v116, v2, v1, s55
	v_cvt_pknorm_u16_f32 v1, v164, v165
	v_cvt_pknorm_u16_f32 v2, v166, v167
	s_addc_u32 s15, s5, 0
	v_perm_b32 v117, v2, v1, s55
	v_cvt_pknorm_u16_f32 v1, v168, v169
	v_cvt_pknorm_u16_f32 v2, v170, v171
	s_add_u32 s20, s6, s20
	v_perm_b32 v118, v2, v1, s55
	v_cvt_pknorm_u16_f32 v1, v172, v173
	v_cvt_pknorm_u16_f32 v2, v174, v175
	s_addc_u32 s21, s7, 0
	v_perm_b32 v119, v2, v1, s55
	s_mov_b32 m0, s50
	v_lshl_add_u64 v[2:3], s[14:15], 0, v[200:201]
	global_load_lds_dwordx4 v[2:3], off
	v_lshl_add_u64 v[2:3], s[20:21], 0, v[202:203]
	s_mov_b32 m0, s27
	s_nop 0
	global_load_lds_dwordx4 v[2:3], off
	s_waitcnt lgkmcnt(0)
	v_mfma_scale_f32_32x32x64_f8f6f4 v[64:79], v[184:191], v[112:119], v[64:79], v207, v207 op_sel_hi:[0,0,0]
	ds_read_b128 v[120:123], v221 offset:47104
	ds_read_b128 v[124:127], v222 offset:47104
	v_mfma_scale_f32_32x32x64_f8f6f4 v[48:63], v[224:231], v[112:119], v[48:63], v207, v207 op_sel_hi:[0,0,0]
	ds_read_b128 v[168:171], v221 offset:49152
	ds_read_b128 v[172:175], v222 offset:49152
	ds_read_b128 v[160:163], v219
	ds_read_b128 v[2:5], v219 offset:4096
	ds_read_b128 v[164:167], v220
	ds_read_b128 v[6:9], v220 offset:4096
	v_mov_b32_e32 v1, v128
	v_max3_f32 v1, v1, v128, v129
	v_max3_f32 v1, v1, v130, v131
	v_max3_f32 v1, v1, v132, v133
	v_max3_f32 v1, v1, v134, v135
	v_max3_f32 v1, v1, v136, v137
	v_max3_f32 v1, v1, v138, v139
	v_max3_f32 v1, v1, v140, v141
	v_max3_f32 v1, v1, v142, v143
	v_mfma_scale_f32_32x32x64_f8f6f4 v[32:47], v[176:183], v[112:119], v[32:47], v207, v207 op_sel_hi:[0,0,0]
	v_max3_f32 v1, v1, v144, v145
	v_max3_f32 v1, v1, v146, v147
	v_max3_f32 v1, v1, v148, v149
	v_max3_f32 v1, v1, v150, v151
	v_max3_f32 v1, v1, v152, v153
	v_max3_f32 v1, v1, v154, v155
	v_max3_f32 v1, v1, v156, v157
	v_max3_f32 v1, v1, v158, v159
	v_cmp_ge_f32_e32 vcc, s53, v1
	s_cmp_eq_u64 vcc, exec
	s_waitcnt lgkmcnt(0)
	v_mfma_scale_f32_32x32x64_f8f6f4 v[16:31], v[120:127], v[112:119], v[16:31], v207, v207 op_sel_hi:[0,0,0]
	v_mfma_scale_f32_32x32x64_f8f6f4 v[80:95], v[168:175], v[112:119], v[80:95], v207, v207 op_sel_hi:[0,0,0]
	s_cbranch_scc0 .LBB0_450
.LBB0_435:
	s_waitcnt vmcnt(4)
	s_waitcnt lgkmcnt(0)
	s_barrier
	v_mfma_scale_f32_32x32x64_f8f6f4 v[112:127], v[160:167], v[192:199], v[96:111], v207, v218 op_sel_hi:[0,0,0]
	ds_read_b128 v[176:179], v221 offset:51200
	ds_read_b128 v[184:187], v221 offset:53248
	ds_read_b128 v[180:183], v222 offset:51200
	ds_read_b128 v[168:171], v221 offset:55296
	ds_read_b128 v[188:191], v222 offset:53248
	ds_read_b128 v[172:175], v222 offset:55296
	v_cvt_pknorm_u16_f32 v1, v128, v129
	v_cvt_pknorm_u16_f32 v10, v130, v131
	v_perm_b32 v160, v10, v1, s55
	v_cvt_pknorm_u16_f32 v1, v132, v133
	v_cvt_pknorm_u16_f32 v10, v134, v135
	v_perm_b32 v161, v10, v1, s55
	v_cvt_pknorm_u16_f32 v1, v136, v137
	v_cvt_pknorm_u16_f32 v10, v138, v139
	v_perm_b32 v162, v10, v1, s55
	v_cvt_pknorm_u16_f32 v1, v140, v141
	v_cvt_pknorm_u16_f32 v10, v142, v143
	v_perm_b32 v163, v10, v1, s55
	v_mfma_scale_f32_32x32x64_f8f6f4 v[128:143], v[2:9], v[192:199], v[96:111], v207, v218 op_sel_hi:[0,0,0]
	s_min_u32 s14, s33, s17
	s_lshl_b32 s20, s14, 13
	v_cvt_pknorm_u16_f32 v1, v144, v145
	v_cvt_pknorm_u16_f32 v2, v146, v147
	s_add_u32 s14, s4, s20
	v_perm_b32 v164, v2, v1, s55
	v_cvt_pknorm_u16_f32 v1, v148, v149
	v_cvt_pknorm_u16_f32 v2, v150, v151
	s_addc_u32 s15, s5, 0
	v_perm_b32 v165, v2, v1, s55
	v_cvt_pknorm_u16_f32 v1, v152, v153
	v_cvt_pknorm_u16_f32 v2, v154, v155
	s_add_u32 s20, s6, s20
	v_perm_b32 v166, v2, v1, s55
	v_cvt_pknorm_u16_f32 v1, v156, v157
	v_cvt_pknorm_u16_f32 v2, v158, v159
	s_addc_u32 s21, s7, 0
	v_perm_b32 v167, v2, v1, s55
	s_mov_b32 m0, s51
	v_lshl_add_u64 v[2:3], s[14:15], 0, v[200:201]
	global_load_lds_dwordx4 v[2:3], off
	v_lshl_add_u64 v[2:3], s[20:21], 0, v[202:203]
	s_mov_b32 m0, s26
	s_nop 0
	global_load_lds_dwordx4 v[2:3], off
	s_waitcnt lgkmcnt(0)
	v_mfma_scale_f32_32x32x64_f8f6f4 v[64:79], v[176:183], v[160:167], v[64:79], v207, v207 op_sel_hi:[0,0,0]
	ds_read_b128 v[2:5], v221 offset:57344
	ds_read_b128 v[6:9], v222 offset:57344
	v_mfma_scale_f32_32x32x64_f8f6f4 v[48:63], v[184:191], v[160:167], v[48:63], v207, v207 op_sel_hi:[0,0,0]
	ds_read_b128 v[144:147], v221 offset:59392
	ds_read_b128 v[148:151], v222 offset:59392
	ds_read_b128 v[184:187], v219 offset:8192
	ds_read_b128 v[176:179], v219 offset:12288
	ds_read_b128 v[188:191], v220 offset:8192
	ds_read_b128 v[180:183], v220 offset:12288
	v_mov_b32_e32 v1, v112
	v_max3_f32 v1, v1, v112, v113
	v_max3_f32 v1, v1, v114, v115
	v_max3_f32 v1, v1, v116, v117
	v_max3_f32 v1, v1, v118, v119
	v_max3_f32 v1, v1, v120, v121
	v_max3_f32 v1, v1, v122, v123
	v_max3_f32 v1, v1, v124, v125
	v_max3_f32 v1, v1, v126, v127
	v_mfma_scale_f32_32x32x64_f8f6f4 v[32:47], v[168:175], v[160:167], v[32:47], v207, v207 op_sel_hi:[0,0,0]
	v_max3_f32 v1, v1, v128, v129
	v_max3_f32 v1, v1, v130, v131
	v_max3_f32 v1, v1, v132, v133
	v_max3_f32 v1, v1, v134, v135
	v_max3_f32 v1, v1, v136, v137
	v_max3_f32 v1, v1, v138, v139
	v_max3_f32 v1, v1, v140, v141
	v_max3_f32 v1, v1, v142, v143
	v_cmp_ge_f32_e32 vcc, s53, v1
	s_cmp_eq_u64 vcc, exec
	s_waitcnt lgkmcnt(0)
	v_mfma_scale_f32_32x32x64_f8f6f4 v[16:31], v[2:9], v[160:167], v[16:31], v207, v207 op_sel_hi:[0,0,0]
	v_mfma_scale_f32_32x32x64_f8f6f4 v[80:95], v[144:151], v[160:167], v[80:95], v207, v207 op_sel_hi:[0,0,0]
	s_cbranch_scc0 .LBB0_453

.LBB0_518:
	s_andn2_saveexec_b64 s[6:7], s[6:7]
	s_cbranch_execz .LBB0_538
	s_mov_b64 s[6:7], exec
	buffer_wbl2 sc1
	buffer_inv sc1
	s_waitcnt lgkmcnt(0)
	s_waitcnt vmcnt(0)
	v_mbcnt_lo_u32_b32 v1, s6, 0
	v_mbcnt_hi_u32_b32 v1, s7, v1
	v_cmp_eq_u32_e32 vcc, 0, v1
	s_and_saveexec_b64 s[10:11], vcc
	s_cbranch_execz .LBB0_521
	s_bcnt1_i32_b64 s3, s[6:7]
	v_mov_b32_e32 v3, s3
	v_mov_b32_e32 v4, 0x3000
	global_atomic_add v3, v4, v3, s[4:5] offset:1024 sc0

.LBB0_533:
	s_or_b64 exec, exec, s[12:13]
	s_and_saveexec_b64 s[6:7], s[16:17]
	s_cbranch_execz .LBB0_535
	v_mov_b32_e32 v1, 1
	global_atomic_add v[2:3], v1, off
	s_add_u32 s2, s4, 0x2400
	s_addc_u32 s3, s5, 0
	v_mov_b32_e32 v4, 0
	v_mov_b32_e32 v5, 1
	global_atomic_add v4, v5, s[2:3]
	global_atomic_add v4, v5, s[2:3] offset:256
	global_atomic_add v4, v5, s[2:3] offset:512
	global_atomic_add v4, v5, s[2:3] offset:768
	global_atomic_add v4, v5, s[2:3] offset:1024
	global_atomic_add v4, v5, s[2:3] offset:1280
	global_atomic_add v4, v5, s[2:3] offset:1536
	global_atomic_add v4, v5, s[2:3] offset:1792
	global_atomic_add v4, v5, s[2:3] offset:2048
	global_atomic_add v4, v5, s[2:3] offset:2304
	global_atomic_add v4, v5, s[2:3] offset:2560
	global_atomic_add v4, v5, s[2:3] offset:2816
	global_atomic_add v4, v5, s[2:3] offset:3072
	global_atomic_add v4, v5, s[2:3] offset:3328
	global_atomic_add v4, v5, s[2:3] offset:3584
	global_atomic_add v4, v5, s[2:3] offset:3840
.LBB0_535:
	s_or_b64 exec, exec, s[6:7]
	s_mov_b64 s[6:7], exec
	v_mbcnt_lo_u32_b32 v1, s6, 0
	v_mbcnt_hi_u32_b32 v1, s7, v1
	v_cmp_eq_u32_e32 vcc, 0, v1
	s_waitcnt vmcnt(0)
	s_and_saveexec_b64 s[12:13], vcc
	s_cbranch_execz .LBB0_537

.LBB0_1023:
	s_or_b64 exec, exec, s[8:9]
	s_and_saveexec_b64 s[6:7], s[10:11]
	s_cbranch_execz .LBB0_1025
	v_mov_b32_e32 v1, 1
	global_atomic_add v[2:3], v1, off
	s_add_u32 s2, s4, 0x2400
	s_addc_u32 s3, s5, 0
	v_mov_b32_e32 v4, 0
	v_mov_b32_e32 v5, 1
	global_atomic_add v4, v5, s[2:3]
	global_atomic_add v4, v5, s[2:3] offset:256
	global_atomic_add v4, v5, s[2:3] offset:512
	global_atomic_add v4, v5, s[2:3] offset:768
	global_atomic_add v4, v5, s[2:3] offset:1024
	global_atomic_add v4, v5, s[2:3] offset:1280
	global_atomic_add v4, v5, s[2:3] offset:1536
	global_atomic_add v4, v5, s[2:3] offset:1792
	global_atomic_add v4, v5, s[2:3] offset:2048
	global_atomic_add v4, v5, s[2:3] offset:2304
	global_atomic_add v4, v5, s[2:3] offset:2560
	global_atomic_add v4, v5, s[2:3] offset:2816
	global_atomic_add v4, v5, s[2:3] offset:3072
	global_atomic_add v4, v5, s[2:3] offset:3328
	global_atomic_add v4, v5, s[2:3] offset:3584
	global_atomic_add v4, v5, s[2:3] offset:3840

.LBB0_1054:
	v_cndmask_b32_e64 v4, 0, 1, s[90:91]
	v_cmp_ne_u32_e64 s[4:5], 1, v4
	s_andn2_b64 vcc, exec, s[90:91]
	v_mov_b32_e32 v202, v174
	v_mov_b32_e32 v200, v172
	v_mov_b32_e32 v203, v170
	v_mov_b32_e32 v201, v168
	v_mov_b64_e32 v[166:167], v[2:3]
	s_mov_b32 s100, 0
	s_cbranch_vccnz .LBB0_1056
	v_lshlrev_b32_e32 v4, 2, v198
	v_add_u32_e32 v4, 0, v4
	ds_read_b32 v8, v4 offset:160
	v_lshlrev_b32_e32 v9, 8, v199
	v_add_u32_e32 v4, v9, v1
	s_mov_b32 s19, 0x22000
	v_add_u32_e32 v10, 0x80, v4
	s_waitcnt lgkmcnt(0)
	v_cmp_lt_i32_e32 vcc, v4, v8
	v_mul_hi_i32 v7, v198, s19
	v_mul_lo_u32 v6, v198, s19
	v_cndmask_b32_e32 v4, v9, v4, vcc
	v_ashrrev_i32_e32 v5, 31, v4
	v_lshl_add_u64 v[6:7], s[82:83], 0, v[6:7]
	v_lshl_add_u64 v[4:5], v[4:5], 2, v[6:7]
	v_cmp_lt_i32_e32 vcc, v10, v8
	global_load_dword v200, v[4:5], off
	s_mov_b32 s19, 0x180000
	v_cndmask_b32_e32 v4, v9, v10, vcc
	v_ashrrev_i32_e32 v5, 31, v4
	v_lshl_add_u64 v[4:5], v[4:5], 2, v[6:7]
	global_load_dword v201, v[4:5], off
	s_ashr_i32 s23, s22, 31
	s_lshl_b64 s[62:63], s[22:23], 18
	s_mov_b32 s44, 0x22000
	v_add_u32_e32 v4, v9, v192
	v_cmp_lt_i32_e32 vcc, v4, v8
	v_add_u32_e32 v10, 0x80, v4
	s_nop 0
	v_cndmask_b32_e32 v4, v9, v4, vcc
	v_ashrrev_i32_e32 v5, 31, v4
	v_lshl_add_u64 v[4:5], v[4:5], 2, v[6:7]
	v_cmp_lt_i32_e32 vcc, v10, v8
	global_load_dword v202, v[4:5], off
	s_nop 0
	v_cndmask_b32_e32 v4, v9, v10, vcc
	v_ashrrev_i32_e32 v5, 31, v4
	v_lshl_add_u64 v[4:5], v[4:5], 2, v[6:7]
	global_load_dword v203, v[4:5], off
	v_mul_hi_i32 v5, v198, s19
	v_mul_lo_u32 v4, v198, s19
	v_lshl_add_u64 v[4:5], s[10:11], 0, v[4:5]
	v_lshl_add_u64 v[166:167], v[4:5], 0, s[62:63]
	s_mov_b32 s100, 1

.LBB0_1058:
	s_or_b64 exec, exec, s[96:97]
	s_cmp_eq_u32 s100, 0
	s_cbranch_scc1 .Le1_tok_done
	s_mov_b32 s100, 0
	s_waitcnt vmcnt(8)
	v_lshlrev_b32_e32 v200, 9, v200
	v_lshlrev_b32_e32 v201, 9, v201
	v_lshlrev_b32_e32 v202, 9, v202
	v_lshlrev_b32_e32 v203, 9, v203
	v_and_b32_e32 v200, 0xfffffc00, v200
	v_and_b32_e32 v201, 0xfffffc00, v201
	v_and_b32_e32 v202, 0xfffffc00, v202
	v_and_b32_e32 v203, 0xfffffc00, v203
	v_add_u32_e32 v200, v200, v194
	v_add_u32_e32 v201, v201, v194
	v_add_u32_e32 v202, v202, v195
	v_add_u32_e32 v203, v203, v195
.Le1_tok_done:
	s_andn2_b64 s[18:19], s[88:89], exec
	s_and_b64 s[62:63], s[92:93], exec
	s_add_i32 s23, s23, 2
	s_or_b64 s[88:89], s[18:19], s[62:63]
	s_cmp_gt_u32 s23, 5
	s_cbranch_scc1 .LBB0_1062

.LBB0_1125:
	v_lshlrev_b32_e32 v2, 2, v220
	s_nop 15
	s_nop 15
	v_add_u32_e32 v2, 0, v2
	ds_read_b32 v14, v2 offset:160
	v_lshlrev_b32_e32 v16, 8, v221
	v_add_u32_e32 v2, v16, v185
	s_waitcnt lgkmcnt(0)
	v_cmp_lt_i32_e64 s[16:17], v2, v14
	s_nop 1
	v_cndmask_b32_e64 v2, v16, v2, s[16:17]
	v_ashrrev_i32_e32 v3, 31, v2
	v_mad_i64_i32 v[4:5], s[4:5], v220, s31, v[2:3]
	v_lshl_add_u64 v[2:3], v[4:5], 2, s[82:83]
	global_load_dword v24, v[2:3], off
	v_lshl_add_u64 v[2:3], v[4:5], 2, s[90:91]
	global_load_dword v224, v[2:3], off
	v_add_u32_e32 v2, v16, v223
	v_cmp_lt_i32_e32 vcc, v2, v14
	s_nop 1
	v_cndmask_b32_e32 v2, v16, v2, vcc
	v_ashrrev_i32_e32 v3, 31, v2
	v_mad_i64_i32 v[2:3], s[4:5], v220, s31, v[2:3]
	v_lshlrev_b64 v[2:3], 2, v[2:3]
	v_lshl_add_u64 v[6:7], s[82:83], 0, v[2:3]
	v_lshl_add_u64 v[2:3], s[90:91], 0, v[2:3]
	global_load_dword v8, v[6:7], off
	global_load_dword v17, v[2:3], off
	v_add_u32_e32 v2, v16, v216
	v_cmp_lt_i32_e64 s[4:5], v2, v14
	s_nop 1
	v_cndmask_b32_e64 v2, v16, v2, s[4:5]
	v_ashrrev_i32_e32 v3, 31, v2
	v_mad_i64_i32 v[2:3], s[6:7], v220, s31, v[2:3]
	v_lshlrev_b64 v[2:3], 2, v[2:3]
	v_lshl_add_u64 v[6:7], s[82:83], 0, v[2:3]
	v_lshl_add_u64 v[2:3], s[90:91], 0, v[2:3]
	global_load_dword v10, v[6:7], off
	global_load_dword v15, v[2:3], off
	v_add_u32_e32 v2, v16, v212
	v_cmp_lt_i32_e64 s[6:7], v2, v14
	s_nop 1
	v_cndmask_b32_e64 v2, v16, v2, s[6:7]
	v_ashrrev_i32_e32 v3, 31, v2
	v_mad_i64_i32 v[2:3], s[8:9], v220, s31, v[2:3]
	v_lshlrev_b64 v[2:3], 2, v[2:3]
	v_lshl_add_u64 v[6:7], s[82:83], 0, v[2:3]
	v_lshl_add_u64 v[2:3], s[90:91], 0, v[2:3]
	global_load_dword v12, v[6:7], off
	global_load_dword v13, v[2:3], off
	v_add_u32_e32 v2, v16, v250
	v_cmp_lt_i32_e64 s[8:9], v2, v14
	s_nop 1
	v_cndmask_b32_e64 v2, v16, v2, s[8:9]
	v_ashrrev_i32_e32 v3, 31, v2
	v_mad_i64_i32 v[2:3], s[10:11], v220, s31, v[2:3]
	v_lshlrev_b64 v[2:3], 2, v[2:3]
	v_lshl_add_u64 v[6:7], s[82:83], 0, v[2:3]
	v_lshl_add_u64 v[2:3], s[90:91], 0, v[2:3]
	global_load_dword v20, v[6:7], off
	global_load_dword v11, v[2:3], off
	v_add_u32_e32 v2, v16, v251
	v_cmp_lt_i32_e64 s[10:11], v2, v14
	s_nop 1
	v_cndmask_b32_e64 v2, v16, v2, s[10:11]
	v_ashrrev_i32_e32 v3, 31, v2
	v_mad_i64_i32 v[2:3], s[12:13], v220, s31, v[2:3]
	v_lshlrev_b64 v[2:3], 2, v[2:3]
	v_lshl_add_u64 v[6:7], s[82:83], 0, v[2:3]
	v_lshl_add_u64 v[2:3], s[90:91], 0, v[2:3]
	global_load_dword v21, v[6:7], off
	global_load_dword v9, v[2:3], off
	v_add_u32_e32 v2, v16, v252
	v_cmp_lt_i32_e64 s[12:13], v2, v14
	s_nop 1
	v_cndmask_b32_e64 v2, v16, v2, s[12:13]
	v_ashrrev_i32_e32 v3, 31, v2
	v_mad_i64_i32 v[2:3], s[14:15], v220, s31, v[2:3]
	v_lshlrev_b64 v[2:3], 2, v[2:3]
	v_lshl_add_u64 v[6:7], s[82:83], 0, v[2:3]
	v_lshl_add_u64 v[2:3], s[90:91], 0, v[2:3]
	global_load_dword v22, v[6:7], off
	global_load_dword v19, v[2:3], off
	v_add_u32_e32 v2, v16, v253
	v_cmp_lt_i32_e64 s[14:15], v2, v14
	s_nop 1
	v_cndmask_b32_e64 v2, v16, v2, s[14:15]
	v_ashrrev_i32_e32 v3, 31, v2
	v_mad_i64_i32 v[2:3], s[62:63], v220, s31, v[2:3]
	v_lshlrev_b64 v[2:3], 2, v[2:3]
	v_lshl_add_u64 v[6:7], s[82:83], 0, v[2:3]
	v_lshl_add_u64 v[2:3], s[90:91], 0, v[2:3]
	global_load_dword v23, v[6:7], off
	global_load_dword v18, v[2:3], off
	s_waitcnt vmcnt(0)
	v_cndmask_b32_e64 v6, -1, v24, s[16:17]
	v_lshl_or_b32 v2, s22, 8, v254
	v_ashrrev_i32_e32 v3, 31, v2
	v_cmp_lt_i32_e64 s[16:17], -1, v6
	s_and_saveexec_b64 s[22:23], s[16:17]
	s_cbranch_execz .LBB0_1127
	v_mov_b32_e32 v7, v0
	v_mul_f32_e32 v14, 0.5, v224
	v_lshlrev_b64 v[4:5], 10, v[6:7]
	v_lshl_add_u64 v[24:25], s[92:93], 0, v[4:5]
	v_pk_mul_f32 v[26:27], v[158:159], v[14:15] op_sel_hi:[1,0]
	v_pk_mul_f32 v[30:31], v[154:155], v[14:15] op_sel_hi:[1,0]
	v_mov_b32_e32 v4, v0
	v_mov_b32_e32 v5, v0
	v_cvt_pk_fp8_f32 v4, v26, v27
	v_cvt_pk_fp8_f32 v5, v30, v31
	v_pk_mul_f32 v[6:7], v[160:161], v[14:15] op_sel_hi:[1,0]
	v_pk_mul_f32 v[28:29], v[156:157], v[14:15] op_sel_hi:[1,0]
	v_cvt_pk_fp8_f32 v4, v6, v7 op_sel:[0,0,1]
	v_cvt_pk_fp8_f32 v5, v28, v29 op_sel:[0,0,1]
	v_pk_mul_f32 v[28:29], v[150:151], v[14:15] op_sel_hi:[1,0]
	v_pk_mul_f32 v[32:33], v[146:147], v[14:15] op_sel_hi:[1,0]
	v_mov_b32_e32 v6, v0
	v_mov_b32_e32 v7, v0
	v_cvt_pk_fp8_f32 v6, v28, v29
	v_cvt_pk_fp8_f32 v7, v32, v33
	v_pk_mul_f32 v[26:27], v[152:153], v[14:15] op_sel_hi:[1,0]
	v_pk_mul_f32 v[30:31], v[148:149], v[14:15] op_sel_hi:[1,0]
	v_cvt_pk_fp8_f32 v6, v26, v27 op_sel:[0,0,1]
	v_cvt_pk_fp8_f32 v7, v30, v31 op_sel:[0,0,1]
	v_lshl_add_u64 v[24:25], v[24:25], 0, v[2:3]
	v_lshl_add_u64 v[24:25], v[24:25], 0, v[170:171]
	v_permlane16_swap_b32_e32 v4, v6
	v_permlane16_swap_b32_e32 v5, v7
	global_store_dwordx4 v[24:25], v[4:7], off

.LBB0_1177:
	s_mov_b64 s[6:7], exec
	buffer_wbl2 sc1
	buffer_inv sc1
	s_waitcnt lgkmcnt(0)
	s_waitcnt vmcnt(0)
	v_mbcnt_lo_u32_b32 v1, s6, 0
	v_mbcnt_hi_u32_b32 v1, s7, v1
	v_cmp_eq_u32_e32 vcc, 0, v1
	s_and_saveexec_b64 s[8:9], vcc
	s_cbranch_execz .LBB0_1179
	s_bcnt1_i32_b64 s3, s[6:7]
	v_mov_b32_e32 v3, s3
	v_mov_b32_e32 v4, 0x3000
	global_atomic_add v3, v4, v3, s[4:5] offset:1024 sc0

.LBB0_1193:
	s_or_b64 exec, exec, s[6:7]
	s_mov_b64 s[6:7], exec
	v_mbcnt_lo_u32_b32 v1, s6, 0
	v_mbcnt_hi_u32_b32 v1, s7, v1
	v_cmp_eq_u32_e32 vcc, 0, v1
	s_waitcnt vmcnt(0)
	s_and_saveexec_b64 s[8:9], vcc
	s_cbranch_execnz .LBB0_1194
	s_getpc_b64 s[98:99]

.LBB0_1194:
	s_getpc_b64 s[98:99]

	.amdhsa_kernel _Z10fwd_kernel6Params
		.amdhsa_group_segment_fixed_size 0
		.amdhsa_private_segment_fixed_size 0
		.amdhsa_kernarg_size 456
		.amdhsa_user_sgpr_count 2
		.amdhsa_user_sgpr_dispatch_ptr 0
		.amdhsa_user_sgpr_queue_ptr 0
		.amdhsa_user_sgpr_kernarg_segment_ptr 1
		.amdhsa_user_sgpr_dispatch_id 0
		.amdhsa_user_sgpr_kernarg_preload_length 0
		.amdhsa_user_sgpr_kernarg_preload_offset 0
		.amdhsa_user_sgpr_private_segment_size 0
		.amdhsa_uses_dynamic_stack 0
		.amdhsa_enable_private_segment 0
		.amdhsa_system_sgpr_workgroup_id_x 1
		.amdhsa_system_sgpr_workgroup_id_y 0
		.amdhsa_system_sgpr_workgroup_id_z 0
		.amdhsa_system_sgpr_workgroup_info 0
		.amdhsa_system_vgpr_workitem_id 0
		.amdhsa_next_free_vgpr 256
		.amdhsa_next_free_sgpr 102
		.amdhsa_accum_offset 256
		.amdhsa_reserve_vcc 1
		.amdhsa_float_round_mode_32 0
		.amdhsa_float_round_mode_16_64 0
		.amdhsa_float_denorm_mode_32 3
		.amdhsa_float_denorm_mode_16_64 3
		.amdhsa_dx10_clamp 1
		.amdhsa_ieee_mode 1
		.amdhsa_fp16_overflow 0
		.amdhsa_tg_split 0
		.amdhsa_exception_fp_ieee_invalid_op 0
		.amdhsa_exception_fp_denorm_src 0
		.amdhsa_exception_fp_ieee_div_zero 0
		.amdhsa_exception_fp_ieee_overflow 0
		.amdhsa_exception_fp_ieee_underflow 0
		.amdhsa_exception_fp_ieee_inexact 0
		.amdhsa_exception_int_div_zero 0
	.end_amdhsa_kernel

amdhsa.kernels:
  - .agpr_count:     0
    .args:
      - .offset:         0
        .size:           200
        .value_kind:     by_value
      - .offset:         200
        .size:           4
        .value_kind:     hidden_block_count_x
      - .offset:         204
        .size:           4
        .value_kind:     hidden_block_count_y
      - .offset:         208
        .size:           4
        .value_kind:     hidden_block_count_z
      - .offset:         212
        .size:           2
        .value_kind:     hidden_group_size_x
      - .offset:         214
        .size:           2
        .value_kind:     hidden_group_size_y
      - .offset:         216
        .size:           2
        .value_kind:     hidden_group_size_z
      - .offset:         218
        .size:           2
        .value_kind:     hidden_remainder_x
      - .offset:         220
        .size:           2
        .value_kind:     hidden_remainder_y
      - .offset:         222
        .size:           2
        .value_kind:     hidden_remainder_z
      - .offset:         240
        .size:           8
        .value_kind:     hidden_global_offset_x
      - .offset:         248
        .size:           8
        .value_kind:     hidden_global_offset_y
      - .offset:         256
        .size:           8
        .value_kind:     hidden_global_offset_z
      - .offset:         264
        .size:           2
        .value_kind:     hidden_grid_dims
      - .offset:         320
        .size:           4
        .value_kind:     hidden_dynamic_lds_size
    .group_segment_fixed_size: 0
    .kernarg_segment_align: 8
    .kernarg_segment_size: 456
    .language:       OpenCL C
    .language_version:
      - 2
      - 0
    .max_flat_workgroup_size: 512
    .name:           _Z10fwd_kernel6Params
    .private_segment_fixed_size: 0
    .sgpr_count:     108
    .sgpr_spill_count: 49
    .symbol:         _Z10fwd_kernel6Params.kd
    .uniform_work_group_size: 1
    .uses_dynamic_stack: false
    .vgpr_count:     256
    .vgpr_spill_count: 0
    .wavefront_size: 64
